# full grid barriers: the last XCD leader bumps all eight per-XCD generations directly (one release hop instead of two)
# baseline (speedup 1.0000x reference)
; __device__ __forceinline__ unsigned xb_ld(unsigned* p)              { return __hip_atomic_load(p, __ATOMIC_RELAXED, __HIP_MEMORY_SCOPE_AGENT); }
; __device__ __forceinline__ unsigned xb_add(unsigned* p, unsigned v) { return __hip_atomic_fetch_add(p, v, __ATOMIC_RELAXED, __HIP_MEMORY_SCOPE_AGENT); }
; #define XB_SPIN(cond, bar) do { unsigned _sp = 0; while (cond) { __builtin_amdgcn_s_sleep(1); \
;     if ((++_sp & 255u) == 0u) { if (xb_ld(&(bar)[XB_TMO])) break; if (_sp > XB_SPIN_CAP) { atomicAdd(&(bar)[XB_TMO], 1u); break; } } } } while (0)
; __device__ __forceinline__ void xcd_barrier(const XcdBarrier& b) {
;     ...
;             asm volatile("s_waitcnt vmcnt(0)" ::: "memory");
;             const unsigned og = xb_add(&bar[XB_TOP], 1u);
;             const unsigned tg = og / nx;
;             if (og + 1u == (tg + 1u) * nx) xb_add(&bar[XB_TOPGEN], 1u);
;             else XB_SPIN(xb_ld(&bar[XB_TOPGEN]) == tg, bar);
.LBB0_813:
	s_or_b64 exec, exec, s[8:9]
	s_waitcnt vmcnt(0)
	v_readfirstlane_b32 s6, v4
	v_sub_u32_e32 v4, 0, v2
	s_mov_b64 s[10:11], -1
	v_add_u32_e32 v0, s6, v1
	v_cvt_f32_u32_e32 v1, v2
	s_add_u32 s6, s4, 0x7500
	s_addc_u32 s7, s5, 0
	v_rcp_iflag_f32_e32 v1, v1
	s_nop 0
	v_mul_f32_e32 v1, 0x4f7ffffe, v1
	v_cvt_u32_f32_e32 v1, v1
	v_mul_lo_u32 v4, v4, v1
	v_mul_hi_u32 v4, v1, v4
	v_add_u32_e32 v1, v1, v4
	v_mul_hi_u32 v1, v0, v1
	v_mul_lo_u32 v4, v1, v2
	v_sub_u32_e32 v4, v0, v4
	v_cmp_ge_u32_e32 vcc, v4, v2
	v_add_u32_e32 v5, 1, v1
	v_add_u32_e32 v0, 1, v0
	v_cndmask_b32_e32 v1, v1, v5, vcc
	v_sub_u32_e32 v5, v4, v2
	v_cndmask_b32_e32 v4, v4, v5, vcc
	v_cmp_ge_u32_e32 vcc, v4, v2
	v_add_u32_e32 v4, 1, v1
	s_nop 0
	v_cndmask_b32_e32 v1, v1, v4, vcc
	v_mul_lo_u32 v4, v2, v1
	v_add_u32_e32 v2, v4, v2
	v_cmp_ne_u32_e32 vcc, v0, v2
	v_mov_b64_e32 v[4:5], s[6:7]
	s_and_b64 s[98:99], vcc, exec
	s_and_saveexec_b64 s[8:9], vcc
	s_cbranch_execz .LBB0_825
	global_load_dword v0, v3, s[6:7] sc1
	s_mov_b64 s[14:15], 0
	s_waitcnt vmcnt(0)
	v_cmp_eq_u32_e32 vcc, v0, v1
	s_and_saveexec_b64 s[12:13], vcc
	s_cbranch_execz .LBB0_824
	s_add_u32 s10, s4, 0x4200
	s_addc_u32 s11, s5, 0
	s_mov_b32 s22, 1
	s_mov_b64 s[4:5], 0
	s_branch .LBB0_817

; __device__ __forceinline__ unsigned xb_add(unsigned* p, unsigned v) { return __hip_atomic_fetch_add(p, v, __ATOMIC_RELAXED, __HIP_MEMORY_SCOPE_AGENT); }
; __device__ __forceinline__ void xcd_barrier(const XcdBarrier& b) {
;     ...
;             __builtin_amdgcn_fence(__ATOMIC_ACQUIRE, XB_SCOPE);
;             xb_add(&bar[XB_XGEN(b.x)], 1u);
;             asm volatile("s_waitcnt vmcnt(0)" ::: "memory");
.LBB0_827:
	s_or_b64 exec, exec, s[4:5]
	s_mov_b64 s[4:5], exec
	v_mbcnt_lo_u32_b32 v0, s4, 0
	v_mbcnt_hi_u32_b32 v0, s5, v0
	v_cmp_eq_u32_e32 vcc, 0, v0
	s_waitcnt vmcnt(0)
	s_nop 0
	s_and_saveexec_b64 s[6:7], vcc
	s_cbranch_execz .LBB0_829
	s_cmp_lg_u64 s[98:99], 0
	s_cbranch_scc1 .Lmy_nobump_5
	s_add_u32 s8, s24, 0x2400
	s_addc_u32 s9, s25, 0
	s_bcnt1_i32_b64 s4, s[4:5]
	v_mov_b32_e32 v0, s4
	global_atomic_add v3, v0, s[8:9]
	global_atomic_add v3, v0, s[8:9] offset:256
	global_atomic_add v3, v0, s[8:9] offset:512
	global_atomic_add v3, v0, s[8:9] offset:768
	global_atomic_add v3, v0, s[8:9] offset:1024
	global_atomic_add v3, v0, s[8:9] offset:1280
	global_atomic_add v3, v0, s[8:9] offset:1536
	global_atomic_add v3, v0, s[8:9] offset:1792
.Lmy_nobump_5:
.LBB0_829:
	s_or_b64 exec, exec, s[6:7]
	s_waitcnt vmcnt(0)
